# DSA attention: K rows by coalesced LDS-DMA into a swizzled LDS stage, fragments by ds_read_b128 (was 64 separate 16-byte requests per load); V rows via two register sets two steps ahead; tie pass skip
# speedup vs baseline: 1.0176x; 1.0054x over previous
.Ltk_p1_done:
	s_cmp_lg_u32 s10, 0
	s_cbranch_scc1 .Ltk_fin
	v_mov_b32_e32 v110, s11
	v_cmp_eq_u32_e64 s[20:21], v2, v110
	v_cmp_eq_u32_e64 s[22:23], v3, v110
	v_cmp_eq_u32_e64 s[24:25], v4, v110
	v_cmp_eq_u32_e64 s[26:27], v5, v110
	s_or_b64 s[36:37], s[20:21], s[22:23]
	s_or_b64 s[30:31], s[24:25], s[26:27]
	s_or_b64 s[36:37], s[36:37], s[30:31]
	s_cbranch_scc0 .Ltk_p2_g0
	s_bcnt1_i32_b64 s28, s[20:21]
	v_mbcnt_lo_u32_b32 v111, s20, v114
	v_mbcnt_hi_u32_b32 v111, s21, v111
	v_add_u32_e32 v113, 0, v109
	v_lshl_add_u32 v112, v111, 2, s89
	v_cmp_gt_u32_e64 s[36:37], s29, v111
	s_nop 0
	s_and_b64 s[36:37], s[36:37], s[20:21]
	s_mov_b64 exec, s[36:37]
	ds_write_b32 v112, v113
	s_mov_b64 exec, -1
	v_add_u32_e32 v114, s28, v114
	s_bcnt1_i32_b64 s28, s[22:23]
	v_mbcnt_lo_u32_b32 v111, s22, v114
	v_mbcnt_hi_u32_b32 v111, s23, v111
	v_add_u32_e32 v113, 1, v109
	v_lshl_add_u32 v112, v111, 2, s89
	v_cmp_gt_u32_e64 s[36:37], s29, v111
	s_nop 0
	s_and_b64 s[36:37], s[36:37], s[22:23]
	s_mov_b64 exec, s[36:37]
	ds_write_b32 v112, v113
	s_mov_b64 exec, -1
	v_add_u32_e32 v114, s28, v114
	s_bcnt1_i32_b64 s28, s[24:25]
	v_mbcnt_lo_u32_b32 v111, s24, v114
	v_mbcnt_hi_u32_b32 v111, s25, v111
	v_add_u32_e32 v113, 2, v109
	v_lshl_add_u32 v112, v111, 2, s89
	v_cmp_gt_u32_e64 s[36:37], s29, v111
	s_nop 0
	s_and_b64 s[36:37], s[36:37], s[24:25]
	s_mov_b64 exec, s[36:37]
	ds_write_b32 v112, v113
	s_mov_b64 exec, -1
	v_add_u32_e32 v114, s28, v114
	s_bcnt1_i32_b64 s28, s[26:27]
	v_mbcnt_lo_u32_b32 v111, s26, v114
	v_mbcnt_hi_u32_b32 v111, s27, v111
	v_add_u32_e32 v113, 3, v109
	v_lshl_add_u32 v112, v111, 2, s89
	v_cmp_gt_u32_e64 s[36:37], s29, v111
	s_nop 0
	s_and_b64 s[36:37], s[36:37], s[26:27]
	s_mov_b64 exec, s[36:37]
	ds_write_b32 v112, v113
	s_mov_b64 exec, -1
	v_add_u32_e32 v114, s28, v114
.Ltk_p2_g0:
	v_cmp_eq_u32_e64 s[20:21], v6, v110
	v_cmp_eq_u32_e64 s[22:23], v7, v110
	v_cmp_eq_u32_e64 s[24:25], v8, v110
	v_cmp_eq_u32_e64 s[26:27], v9, v110
	s_or_b64 s[36:37], s[20:21], s[22:23]
	s_or_b64 s[30:31], s[24:25], s[26:27]
	s_or_b64 s[36:37], s[36:37], s[30:31]
	s_cbranch_scc0 .Ltk_p2_g1
	s_bcnt1_i32_b64 s28, s[20:21]
	v_mbcnt_lo_u32_b32 v111, s20, v114
	v_mbcnt_hi_u32_b32 v111, s21, v111
	v_add_u32_e32 v113, 0x100, v109
	v_lshl_add_u32 v112, v111, 2, s89
	v_cmp_gt_u32_e64 s[36:37], s29, v111
	s_nop 0
	s_and_b64 s[36:37], s[36:37], s[20:21]
	s_mov_b64 exec, s[36:37]
	ds_write_b32 v112, v113
	s_mov_b64 exec, -1
	v_add_u32_e32 v114, s28, v114
	s_bcnt1_i32_b64 s28, s[22:23]
	v_mbcnt_lo_u32_b32 v111, s22, v114
	v_mbcnt_hi_u32_b32 v111, s23, v111
	v_add_u32_e32 v113, 0x101, v109
	v_lshl_add_u32 v112, v111, 2, s89
	v_cmp_gt_u32_e64 s[36:37], s29, v111
	s_nop 0
	s_and_b64 s[36:37], s[36:37], s[22:23]
	s_mov_b64 exec, s[36:37]
	ds_write_b32 v112, v113
	s_mov_b64 exec, -1
	v_add_u32_e32 v114, s28, v114
	s_bcnt1_i32_b64 s28, s[24:25]
	v_mbcnt_lo_u32_b32 v111, s24, v114
	v_mbcnt_hi_u32_b32 v111, s25, v111
	v_add_u32_e32 v113, 0x102, v109
	v_lshl_add_u32 v112, v111, 2, s89
	v_cmp_gt_u32_e64 s[36:37], s29, v111
	s_nop 0
	s_and_b64 s[36:37], s[36:37], s[24:25]
	s_mov_b64 exec, s[36:37]
	ds_write_b32 v112, v113
	s_mov_b64 exec, -1
	v_add_u32_e32 v114, s28, v114
	s_bcnt1_i32_b64 s28, s[26:27]
	v_mbcnt_lo_u32_b32 v111, s26, v114
	v_mbcnt_hi_u32_b32 v111, s27, v111
	v_add_u32_e32 v113, 0x103, v109
	v_lshl_add_u32 v112, v111, 2, s89
	v_cmp_gt_u32_e64 s[36:37], s29, v111
	s_nop 0
	s_and_b64 s[36:37], s[36:37], s[26:27]
	s_mov_b64 exec, s[36:37]
	ds_write_b32 v112, v113
	s_mov_b64 exec, -1
	v_add_u32_e32 v114, s28, v114
.Ltk_p2_g1:
	s_cmp_lt_u32 s0, 2
	s_cbranch_scc1 .Ltk_p2_done
	v_cmp_eq_u32_e64 s[20:21], v10, v110
	v_cmp_eq_u32_e64 s[22:23], v11, v110
	v_cmp_eq_u32_e64 s[24:25], v12, v110
	v_cmp_eq_u32_e64 s[26:27], v13, v110
	s_or_b64 s[36:37], s[20:21], s[22:23]
	s_or_b64 s[30:31], s[24:25], s[26:27]
	s_or_b64 s[36:37], s[36:37], s[30:31]
	s_cbranch_scc0 .Ltk_p2_g2
	s_bcnt1_i32_b64 s28, s[20:21]
	v_mbcnt_lo_u32_b32 v111, s20, v114
	v_mbcnt_hi_u32_b32 v111, s21, v111
	v_add_u32_e32 v113, 0x200, v109
	v_lshl_add_u32 v112, v111, 2, s89
	v_cmp_gt_u32_e64 s[36:37], s29, v111
	s_nop 0
	s_and_b64 s[36:37], s[36:37], s[20:21]
	s_mov_b64 exec, s[36:37]
	ds_write_b32 v112, v113
	s_mov_b64 exec, -1
	v_add_u32_e32 v114, s28, v114
	s_bcnt1_i32_b64 s28, s[22:23]
	v_mbcnt_lo_u32_b32 v111, s22, v114
	v_mbcnt_hi_u32_b32 v111, s23, v111
	v_add_u32_e32 v113, 0x201, v109
	v_lshl_add_u32 v112, v111, 2, s89
	v_cmp_gt_u32_e64 s[36:37], s29, v111
	s_nop 0
	s_and_b64 s[36:37], s[36:37], s[22:23]
	s_mov_b64 exec, s[36:37]
	ds_write_b32 v112, v113
	s_mov_b64 exec, -1
	v_add_u32_e32 v114, s28, v114
	s_bcnt1_i32_b64 s28, s[24:25]
	v_mbcnt_lo_u32_b32 v111, s24, v114
	v_mbcnt_hi_u32_b32 v111, s25, v111
	v_add_u32_e32 v113, 0x202, v109
	v_lshl_add_u32 v112, v111, 2, s89
	v_cmp_gt_u32_e64 s[36:37], s29, v111
	s_nop 0
	s_and_b64 s[36:37], s[36:37], s[24:25]
	s_mov_b64 exec, s[36:37]
	ds_write_b32 v112, v113
	s_mov_b64 exec, -1
	v_add_u32_e32 v114, s28, v114
	s_bcnt1_i32_b64 s28, s[26:27]
	v_mbcnt_lo_u32_b32 v111, s26, v114
	v_mbcnt_hi_u32_b32 v111, s27, v111
	v_add_u32_e32 v113, 0x203, v109
	v_lshl_add_u32 v112, v111, 2, s89
	v_cmp_gt_u32_e64 s[36:37], s29, v111
	s_nop 0
	s_and_b64 s[36:37], s[36:37], s[26:27]
	s_mov_b64 exec, s[36:37]
	ds_write_b32 v112, v113
	s_mov_b64 exec, -1
	v_add_u32_e32 v114, s28, v114
.Ltk_p2_g2:
	s_cmp_lt_u32 s0, 3
	s_cbranch_scc1 .Ltk_p2_done
	v_cmp_eq_u32_e64 s[20:21], v14, v110
	v_cmp_eq_u32_e64 s[22:23], v15, v110
	v_cmp_eq_u32_e64 s[24:25], v16, v110
	v_cmp_eq_u32_e64 s[26:27], v17, v110
	s_or_b64 s[36:37], s[20:21], s[22:23]
	s_or_b64 s[30:31], s[24:25], s[26:27]
	s_or_b64 s[36:37], s[36:37], s[30:31]
	s_cbranch_scc0 .Ltk_p2_g3
	s_bcnt1_i32_b64 s28, s[20:21]
	v_mbcnt_lo_u32_b32 v111, s20, v114
	v_mbcnt_hi_u32_b32 v111, s21, v111
	v_add_u32_e32 v113, 0x300, v109
	v_lshl_add_u32 v112, v111, 2, s89
	v_cmp_gt_u32_e64 s[36:37], s29, v111
	s_nop 0
	s_and_b64 s[36:37], s[36:37], s[20:21]
	s_mov_b64 exec, s[36:37]
	ds_write_b32 v112, v113
	s_mov_b64 exec, -1
	v_add_u32_e32 v114, s28, v114
	s_bcnt1_i32_b64 s28, s[22:23]
	v_mbcnt_lo_u32_b32 v111, s22, v114
	v_mbcnt_hi_u32_b32 v111, s23, v111
	v_add_u32_e32 v113, 0x301, v109
	v_lshl_add_u32 v112, v111, 2, s89
	v_cmp_gt_u32_e64 s[36:37], s29, v111
	s_nop 0
	s_and_b64 s[36:37], s[36:37], s[22:23]
	s_mov_b64 exec, s[36:37]
	ds_write_b32 v112, v113
	s_mov_b64 exec, -1
	v_add_u32_e32 v114, s28, v114
	s_bcnt1_i32_b64 s28, s[24:25]
	v_mbcnt_lo_u32_b32 v111, s24, v114
	v_mbcnt_hi_u32_b32 v111, s25, v111
	v_add_u32_e32 v113, 0x302, v109
	v_lshl_add_u32 v112, v111, 2, s89
	v_cmp_gt_u32_e64 s[36:37], s29, v111
	s_nop 0
	s_and_b64 s[36:37], s[36:37], s[24:25]
	s_mov_b64 exec, s[36:37]
	ds_write_b32 v112, v113
	s_mov_b64 exec, -1
	v_add_u32_e32 v114, s28, v114
	s_bcnt1_i32_b64 s28, s[26:27]
	v_mbcnt_lo_u32_b32 v111, s26, v114
	v_mbcnt_hi_u32_b32 v111, s27, v111
	v_add_u32_e32 v113, 0x303, v109
	v_lshl_add_u32 v112, v111, 2, s89
	v_cmp_gt_u32_e64 s[36:37], s29, v111
	s_nop 0
	s_and_b64 s[36:37], s[36:37], s[26:27]
	s_mov_b64 exec, s[36:37]
	ds_write_b32 v112, v113
	s_mov_b64 exec, -1
	v_add_u32_e32 v114, s28, v114
.Ltk_p2_g3:
	s_cmp_lt_u32 s0, 4
	s_cbranch_scc1 .Ltk_p2_done
	v_cmp_eq_u32_e64 s[20:21], v18, v110
	v_cmp_eq_u32_e64 s[22:23], v19, v110
	v_cmp_eq_u32_e64 s[24:25], v20, v110
	v_cmp_eq_u32_e64 s[26:27], v21, v110
	s_or_b64 s[36:37], s[20:21], s[22:23]
	s_or_b64 s[30:31], s[24:25], s[26:27]
	s_or_b64 s[36:37], s[36:37], s[30:31]
	s_cbranch_scc0 .Ltk_p2_g4
	s_bcnt1_i32_b64 s28, s[20:21]
	v_mbcnt_lo_u32_b32 v111, s20, v114
	v_mbcnt_hi_u32_b32 v111, s21, v111
	v_add_u32_e32 v113, 0x400, v109
	v_lshl_add_u32 v112, v111, 2, s89
	v_cmp_gt_u32_e64 s[36:37], s29, v111
	s_nop 0
	s_and_b64 s[36:37], s[36:37], s[20:21]
	s_mov_b64 exec, s[36:37]
	ds_write_b32 v112, v113
	s_mov_b64 exec, -1
	v_add_u32_e32 v114, s28, v114
	s_bcnt1_i32_b64 s28, s[22:23]
	v_mbcnt_lo_u32_b32 v111, s22, v114
	v_mbcnt_hi_u32_b32 v111, s23, v111
	v_add_u32_e32 v113, 0x401, v109
	v_lshl_add_u32 v112, v111, 2, s89
	v_cmp_gt_u32_e64 s[36:37], s29, v111
	s_nop 0
	s_and_b64 s[36:37], s[36:37], s[22:23]
	s_mov_b64 exec, s[36:37]
	ds_write_b32 v112, v113
	s_mov_b64 exec, -1
	v_add_u32_e32 v114, s28, v114
	s_bcnt1_i32_b64 s28, s[24:25]
	v_mbcnt_lo_u32_b32 v111, s24, v114
	v_mbcnt_hi_u32_b32 v111, s25, v111
	v_add_u32_e32 v113, 0x402, v109
	v_lshl_add_u32 v112, v111, 2, s89
	v_cmp_gt_u32_e64 s[36:37], s29, v111
	s_nop 0
	s_and_b64 s[36:37], s[36:37], s[24:25]
	s_mov_b64 exec, s[36:37]
	ds_write_b32 v112, v113
	s_mov_b64 exec, -1
	v_add_u32_e32 v114, s28, v114
	s_bcnt1_i32_b64 s28, s[26:27]
	v_mbcnt_lo_u32_b32 v111, s26, v114
	v_mbcnt_hi_u32_b32 v111, s27, v111
	v_add_u32_e32 v113, 0x403, v109
	v_lshl_add_u32 v112, v111, 2, s89
	v_cmp_gt_u32_e64 s[36:37], s29, v111
	s_nop 0
	s_and_b64 s[36:37], s[36:37], s[26:27]
	s_mov_b64 exec, s[36:37]
	ds_write_b32 v112, v113
	s_mov_b64 exec, -1
	v_add_u32_e32 v114, s28, v114
.Ltk_p2_g4:
	s_cmp_lt_u32 s0, 5
	s_cbranch_scc1 .Ltk_p2_done
	v_cmp_eq_u32_e64 s[20:21], v22, v110
	v_cmp_eq_u32_e64 s[22:23], v23, v110
	v_cmp_eq_u32_e64 s[24:25], v24, v110
	v_cmp_eq_u32_e64 s[26:27], v25, v110
	s_or_b64 s[36:37], s[20:21], s[22:23]
	s_or_b64 s[30:31], s[24:25], s[26:27]
	s_or_b64 s[36:37], s[36:37], s[30:31]
	s_cbranch_scc0 .Ltk_p2_g5
	s_bcnt1_i32_b64 s28, s[20:21]
	v_mbcnt_lo_u32_b32 v111, s20, v114
	v_mbcnt_hi_u32_b32 v111, s21, v111
	v_add_u32_e32 v113, 0x500, v109
	v_lshl_add_u32 v112, v111, 2, s89
	v_cmp_gt_u32_e64 s[36:37], s29, v111
	s_nop 0
	s_and_b64 s[36:37], s[36:37], s[20:21]
	s_mov_b64 exec, s[36:37]
	ds_write_b32 v112, v113
	s_mov_b64 exec, -1
	v_add_u32_e32 v114, s28, v114
	s_bcnt1_i32_b64 s28, s[22:23]
	v_mbcnt_lo_u32_b32 v111, s22, v114
	v_mbcnt_hi_u32_b32 v111, s23, v111
	v_add_u32_e32 v113, 0x501, v109
	v_lshl_add_u32 v112, v111, 2, s89
	v_cmp_gt_u32_e64 s[36:37], s29, v111
	s_nop 0
	s_and_b64 s[36:37], s[36:37], s[22:23]
	s_mov_b64 exec, s[36:37]
	ds_write_b32 v112, v113
	s_mov_b64 exec, -1
	v_add_u32_e32 v114, s28, v114
	s_bcnt1_i32_b64 s28, s[24:25]
	v_mbcnt_lo_u32_b32 v111, s24, v114
	v_mbcnt_hi_u32_b32 v111, s25, v111
	v_add_u32_e32 v113, 0x502, v109
	v_lshl_add_u32 v112, v111, 2, s89
	v_cmp_gt_u32_e64 s[36:37], s29, v111
	s_nop 0
	s_and_b64 s[36:37], s[36:37], s[24:25]
	s_mov_b64 exec, s[36:37]
	ds_write_b32 v112, v113
	s_mov_b64 exec, -1
	v_add_u32_e32 v114, s28, v114
	s_bcnt1_i32_b64 s28, s[26:27]
	v_mbcnt_lo_u32_b32 v111, s26, v114
	v_mbcnt_hi_u32_b32 v111, s27, v111
	v_add_u32_e32 v113, 0x503, v109
	v_lshl_add_u32 v112, v111, 2, s89
	v_cmp_gt_u32_e64 s[36:37], s29, v111
	s_nop 0
	s_and_b64 s[36:37], s[36:37], s[26:27]
	s_mov_b64 exec, s[36:37]
	ds_write_b32 v112, v113
	s_mov_b64 exec, -1
	v_add_u32_e32 v114, s28, v114
.Ltk_p2_g5:
	s_cmp_lt_u32 s0, 6
	s_cbranch_scc1 .Ltk_p2_done
	v_cmp_eq_u32_e64 s[20:21], v26, v110
	v_cmp_eq_u32_e64 s[22:23], v27, v110
	v_cmp_eq_u32_e64 s[24:25], v28, v110
	v_cmp_eq_u32_e64 s[26:27], v29, v110
	s_or_b64 s[36:37], s[20:21], s[22:23]
	s_or_b64 s[30:31], s[24:25], s[26:27]
	s_or_b64 s[36:37], s[36:37], s[30:31]
	s_cbranch_scc0 .Ltk_p2_g6
	s_bcnt1_i32_b64 s28, s[20:21]
	v_mbcnt_lo_u32_b32 v111, s20, v114
	v_mbcnt_hi_u32_b32 v111, s21, v111
	v_add_u32_e32 v113, 0x600, v109
	v_lshl_add_u32 v112, v111, 2, s89
	v_cmp_gt_u32_e64 s[36:37], s29, v111
	s_nop 0
	s_and_b64 s[36:37], s[36:37], s[20:21]
	s_mov_b64 exec, s[36:37]
	ds_write_b32 v112, v113
	s_mov_b64 exec, -1
	v_add_u32_e32 v114, s28, v114
	s_bcnt1_i32_b64 s28, s[22:23]
	v_mbcnt_lo_u32_b32 v111, s22, v114
	v_mbcnt_hi_u32_b32 v111, s23, v111
	v_add_u32_e32 v113, 0x601, v109
	v_lshl_add_u32 v112, v111, 2, s89
	v_cmp_gt_u32_e64 s[36:37], s29, v111
	s_nop 0
	s_and_b64 s[36:37], s[36:37], s[22:23]
	s_mov_b64 exec, s[36:37]
	ds_write_b32 v112, v113
	s_mov_b64 exec, -1
	v_add_u32_e32 v114, s28, v114
	s_bcnt1_i32_b64 s28, s[24:25]
	v_mbcnt_lo_u32_b32 v111, s24, v114
	v_mbcnt_hi_u32_b32 v111, s25, v111
	v_add_u32_e32 v113, 0x602, v109
	v_lshl_add_u32 v112, v111, 2, s89
	v_cmp_gt_u32_e64 s[36:37], s29, v111
	s_nop 0
	s_and_b64 s[36:37], s[36:37], s[24:25]
	s_mov_b64 exec, s[36:37]
	ds_write_b32 v112, v113
	s_mov_b64 exec, -1
	v_add_u32_e32 v114, s28, v114
	s_bcnt1_i32_b64 s28, s[26:27]
	v_mbcnt_lo_u32_b32 v111, s26, v114
	v_mbcnt_hi_u32_b32 v111, s27, v111
	v_add_u32_e32 v113, 0x603, v109
	v_lshl_add_u32 v112, v111, 2, s89
	v_cmp_gt_u32_e64 s[36:37], s29, v111
	s_nop 0
	s_and_b64 s[36:37], s[36:37], s[26:27]
	s_mov_b64 exec, s[36:37]
	ds_write_b32 v112, v113
	s_mov_b64 exec, -1
	v_add_u32_e32 v114, s28, v114
.Ltk_p2_g6:
	s_cmp_lt_u32 s0, 7
	s_cbranch_scc1 .Ltk_p2_done
	v_cmp_eq_u32_e64 s[20:21], v30, v110
	v_cmp_eq_u32_e64 s[22:23], v31, v110
	v_cmp_eq_u32_e64 s[24:25], v32, v110
	v_cmp_eq_u32_e64 s[26:27], v33, v110
	s_or_b64 s[36:37], s[20:21], s[22:23]
	s_or_b64 s[30:31], s[24:25], s[26:27]
	s_or_b64 s[36:37], s[36:37], s[30:31]
	s_cbranch_scc0 .Ltk_p2_g7
	s_bcnt1_i32_b64 s28, s[20:21]
	v_mbcnt_lo_u32_b32 v111, s20, v114
	v_mbcnt_hi_u32_b32 v111, s21, v111
	v_add_u32_e32 v113, 0x700, v109
	v_lshl_add_u32 v112, v111, 2, s89
	v_cmp_gt_u32_e64 s[36:37], s29, v111
	s_nop 0
	s_and_b64 s[36:37], s[36:37], s[20:21]
	s_mov_b64 exec, s[36:37]
	ds_write_b32 v112, v113
	s_mov_b64 exec, -1
	v_add_u32_e32 v114, s28, v114
	s_bcnt1_i32_b64 s28, s[22:23]
	v_mbcnt_lo_u32_b32 v111, s22, v114
	v_mbcnt_hi_u32_b32 v111, s23, v111
	v_add_u32_e32 v113, 0x701, v109
	v_lshl_add_u32 v112, v111, 2, s89
	v_cmp_gt_u32_e64 s[36:37], s29, v111
	s_nop 0
	s_and_b64 s[36:37], s[36:37], s[22:23]
	s_mov_b64 exec, s[36:37]
	ds_write_b32 v112, v113
	s_mov_b64 exec, -1
	v_add_u32_e32 v114, s28, v114
	s_bcnt1_i32_b64 s28, s[24:25]
	v_mbcnt_lo_u32_b32 v111, s24, v114
	v_mbcnt_hi_u32_b32 v111, s25, v111
	v_add_u32_e32 v113, 0x702, v109
	v_lshl_add_u32 v112, v111, 2, s89
	v_cmp_gt_u32_e64 s[36:37], s29, v111
	s_nop 0
	s_and_b64 s[36:37], s[36:37], s[24:25]
	s_mov_b64 exec, s[36:37]
	ds_write_b32 v112, v113
	s_mov_b64 exec, -1
	v_add_u32_e32 v114, s28, v114
	s_bcnt1_i32_b64 s28, s[26:27]
	v_mbcnt_lo_u32_b32 v111, s26, v114
	v_mbcnt_hi_u32_b32 v111, s27, v111
	v_add_u32_e32 v113, 0x703, v109
	v_lshl_add_u32 v112, v111, 2, s89
	v_cmp_gt_u32_e64 s[36:37], s29, v111
	s_nop 0
	s_and_b64 s[36:37], s[36:37], s[26:27]
	s_mov_b64 exec, s[36:37]
	ds_write_b32 v112, v113
	s_mov_b64 exec, -1
	v_add_u32_e32 v114, s28, v114
.Ltk_p2_g7:
	s_cmp_lt_u32 s0, 8
	s_cbranch_scc1 .Ltk_p2_done
	v_cmp_eq_u32_e64 s[20:21], v34, v110
	v_cmp_eq_u32_e64 s[22:23], v35, v110
	v_cmp_eq_u32_e64 s[24:25], v36, v110
	v_cmp_eq_u32_e64 s[26:27], v37, v110
	s_or_b64 s[36:37], s[20:21], s[22:23]
	s_or_b64 s[30:31], s[24:25], s[26:27]
	s_or_b64 s[36:37], s[36:37], s[30:31]
	s_cbranch_scc0 .Ltk_p2_g8
	s_bcnt1_i32_b64 s28, s[20:21]
	v_mbcnt_lo_u32_b32 v111, s20, v114
	v_mbcnt_hi_u32_b32 v111, s21, v111
	v_add_u32_e32 v113, 0x800, v109
	v_lshl_add_u32 v112, v111, 2, s89
	v_cmp_gt_u32_e64 s[36:37], s29, v111
	s_nop 0
	s_and_b64 s[36:37], s[36:37], s[20:21]
	s_mov_b64 exec, s[36:37]
	ds_write_b32 v112, v113
	s_mov_b64 exec, -1
	v_add_u32_e32 v114, s28, v114
	s_bcnt1_i32_b64 s28, s[22:23]
	v_mbcnt_lo_u32_b32 v111, s22, v114
	v_mbcnt_hi_u32_b32 v111, s23, v111
	v_add_u32_e32 v113, 0x801, v109
	v_lshl_add_u32 v112, v111, 2, s89
	v_cmp_gt_u32_e64 s[36:37], s29, v111
	s_nop 0
	s_and_b64 s[36:37], s[36:37], s[22:23]
	s_mov_b64 exec, s[36:37]
	ds_write_b32 v112, v113
	s_mov_b64 exec, -1
	v_add_u32_e32 v114, s28, v114
	s_bcnt1_i32_b64 s28, s[24:25]
	v_mbcnt_lo_u32_b32 v111, s24, v114
	v_mbcnt_hi_u32_b32 v111, s25, v111
	v_add_u32_e32 v113, 0x802, v109
	v_lshl_add_u32 v112, v111, 2, s89
	v_cmp_gt_u32_e64 s[36:37], s29, v111
	s_nop 0
	s_and_b64 s[36:37], s[36:37], s[24:25]
	s_mov_b64 exec, s[36:37]
	ds_write_b32 v112, v113
	s_mov_b64 exec, -1
	v_add_u32_e32 v114, s28, v114
	s_bcnt1_i32_b64 s28, s[26:27]
	v_mbcnt_lo_u32_b32 v111, s26, v114
	v_mbcnt_hi_u32_b32 v111, s27, v111
	v_add_u32_e32 v113, 0x803, v109
	v_lshl_add_u32 v112, v111, 2, s89
	v_cmp_gt_u32_e64 s[36:37], s29, v111
	s_nop 0
	s_and_b64 s[36:37], s[36:37], s[26:27]
	s_mov_b64 exec, s[36:37]
	ds_write_b32 v112, v113
	s_mov_b64 exec, -1
	v_add_u32_e32 v114, s28, v114
.Ltk_p2_g8:
	s_cmp_lt_u32 s0, 9
	s_cbranch_scc1 .Ltk_p2_done
	v_cmp_eq_u32_e64 s[20:21], v38, v110
	v_cmp_eq_u32_e64 s[22:23], v39, v110
	v_cmp_eq_u32_e64 s[24:25], v40, v110
	v_cmp_eq_u32_e64 s[26:27], v41, v110
	s_or_b64 s[36:37], s[20:21], s[22:23]
	s_or_b64 s[30:31], s[24:25], s[26:27]
	s_or_b64 s[36:37], s[36:37], s[30:31]
	s_cbranch_scc0 .Ltk_p2_g9
	s_bcnt1_i32_b64 s28, s[20:21]
	v_mbcnt_lo_u32_b32 v111, s20, v114
	v_mbcnt_hi_u32_b32 v111, s21, v111
	v_add_u32_e32 v113, 0x900, v109
	v_lshl_add_u32 v112, v111, 2, s89
	v_cmp_gt_u32_e64 s[36:37], s29, v111
	s_nop 0
	s_and_b64 s[36:37], s[36:37], s[20:21]
	s_mov_b64 exec, s[36:37]
	ds_write_b32 v112, v113
	s_mov_b64 exec, -1
	v_add_u32_e32 v114, s28, v114
	s_bcnt1_i32_b64 s28, s[22:23]
	v_mbcnt_lo_u32_b32 v111, s22, v114
	v_mbcnt_hi_u32_b32 v111, s23, v111
	v_add_u32_e32 v113, 0x901, v109
	v_lshl_add_u32 v112, v111, 2, s89
	v_cmp_gt_u32_e64 s[36:37], s29, v111
	s_nop 0
	s_and_b64 s[36:37], s[36:37], s[22:23]
	s_mov_b64 exec, s[36:37]
	ds_write_b32 v112, v113
	s_mov_b64 exec, -1
	v_add_u32_e32 v114, s28, v114
	s_bcnt1_i32_b64 s28, s[24:25]
	v_mbcnt_lo_u32_b32 v111, s24, v114
	v_mbcnt_hi_u32_b32 v111, s25, v111
	v_add_u32_e32 v113, 0x902, v109
	v_lshl_add_u32 v112, v111, 2, s89
	v_cmp_gt_u32_e64 s[36:37], s29, v111
	s_nop 0
	s_and_b64 s[36:37], s[36:37], s[24:25]
	s_mov_b64 exec, s[36:37]
	ds_write_b32 v112, v113
	s_mov_b64 exec, -1
	v_add_u32_e32 v114, s28, v114
	s_bcnt1_i32_b64 s28, s[26:27]
	v_mbcnt_lo_u32_b32 v111, s26, v114
	v_mbcnt_hi_u32_b32 v111, s27, v111
	v_add_u32_e32 v113, 0x903, v109
	v_lshl_add_u32 v112, v111, 2, s89
	v_cmp_gt_u32_e64 s[36:37], s29, v111
	s_nop 0
	s_and_b64 s[36:37], s[36:37], s[26:27]
	s_mov_b64 exec, s[36:37]
	ds_write_b32 v112, v113
	s_mov_b64 exec, -1
	v_add_u32_e32 v114, s28, v114
.Ltk_p2_g9:
	s_cmp_lt_u32 s0, 10
	s_cbranch_scc1 .Ltk_p2_done
	v_cmp_eq_u32_e64 s[20:21], v42, v110
	v_cmp_eq_u32_e64 s[22:23], v43, v110
	v_cmp_eq_u32_e64 s[24:25], v44, v110
	v_cmp_eq_u32_e64 s[26:27], v45, v110
	s_or_b64 s[36:37], s[20:21], s[22:23]
	s_or_b64 s[30:31], s[24:25], s[26:27]
	s_or_b64 s[36:37], s[36:37], s[30:31]
	s_cbranch_scc0 .Ltk_p2_g10
	s_bcnt1_i32_b64 s28, s[20:21]
	v_mbcnt_lo_u32_b32 v111, s20, v114
	v_mbcnt_hi_u32_b32 v111, s21, v111
	v_add_u32_e32 v113, 0xa00, v109
	v_lshl_add_u32 v112, v111, 2, s89
	v_cmp_gt_u32_e64 s[36:37], s29, v111
	s_nop 0
	s_and_b64 s[36:37], s[36:37], s[20:21]
	s_mov_b64 exec, s[36:37]
	ds_write_b32 v112, v113
	s_mov_b64 exec, -1
	v_add_u32_e32 v114, s28, v114
	s_bcnt1_i32_b64 s28, s[22:23]
	v_mbcnt_lo_u32_b32 v111, s22, v114
	v_mbcnt_hi_u32_b32 v111, s23, v111
	v_add_u32_e32 v113, 0xa01, v109
	v_lshl_add_u32 v112, v111, 2, s89
	v_cmp_gt_u32_e64 s[36:37], s29, v111
	s_nop 0
	s_and_b64 s[36:37], s[36:37], s[22:23]
	s_mov_b64 exec, s[36:37]
	ds_write_b32 v112, v113
	s_mov_b64 exec, -1
	v_add_u32_e32 v114, s28, v114
	s_bcnt1_i32_b64 s28, s[24:25]
	v_mbcnt_lo_u32_b32 v111, s24, v114
	v_mbcnt_hi_u32_b32 v111, s25, v111
	v_add_u32_e32 v113, 0xa02, v109
	v_lshl_add_u32 v112, v111, 2, s89
	v_cmp_gt_u32_e64 s[36:37], s29, v111
	s_nop 0
	s_and_b64 s[36:37], s[36:37], s[24:25]
	s_mov_b64 exec, s[36:37]
	ds_write_b32 v112, v113
	s_mov_b64 exec, -1
	v_add_u32_e32 v114, s28, v114
	s_bcnt1_i32_b64 s28, s[26:27]
	v_mbcnt_lo_u32_b32 v111, s26, v114
	v_mbcnt_hi_u32_b32 v111, s27, v111
	v_add_u32_e32 v113, 0xa03, v109
	v_lshl_add_u32 v112, v111, 2, s89
	v_cmp_gt_u32_e64 s[36:37], s29, v111
	s_nop 0
	s_and_b64 s[36:37], s[36:37], s[26:27]
	s_mov_b64 exec, s[36:37]
	ds_write_b32 v112, v113
	s_mov_b64 exec, -1
	v_add_u32_e32 v114, s28, v114
.Ltk_p2_g10:
	s_cmp_lt_u32 s0, 11
	s_cbranch_scc1 .Ltk_p2_done
	v_cmp_eq_u32_e64 s[20:21], v46, v110
	v_cmp_eq_u32_e64 s[22:23], v47, v110
	v_cmp_eq_u32_e64 s[24:25], v48, v110
	v_cmp_eq_u32_e64 s[26:27], v49, v110
	s_or_b64 s[36:37], s[20:21], s[22:23]
	s_or_b64 s[30:31], s[24:25], s[26:27]
	s_or_b64 s[36:37], s[36:37], s[30:31]
	s_cbranch_scc0 .Ltk_p2_g11
	s_bcnt1_i32_b64 s28, s[20:21]
	v_mbcnt_lo_u32_b32 v111, s20, v114
	v_mbcnt_hi_u32_b32 v111, s21, v111
	v_add_u32_e32 v113, 0xb00, v109
	v_lshl_add_u32 v112, v111, 2, s89
	v_cmp_gt_u32_e64 s[36:37], s29, v111
	s_nop 0
	s_and_b64 s[36:37], s[36:37], s[20:21]
	s_mov_b64 exec, s[36:37]
	ds_write_b32 v112, v113
	s_mov_b64 exec, -1
	v_add_u32_e32 v114, s28, v114
	s_bcnt1_i32_b64 s28, s[22:23]
	v_mbcnt_lo_u32_b32 v111, s22, v114
	v_mbcnt_hi_u32_b32 v111, s23, v111
	v_add_u32_e32 v113, 0xb01, v109
	v_lshl_add_u32 v112, v111, 2, s89
	v_cmp_gt_u32_e64 s[36:37], s29, v111
	s_nop 0
	s_and_b64 s[36:37], s[36:37], s[22:23]
	s_mov_b64 exec, s[36:37]
	ds_write_b32 v112, v113
	s_mov_b64 exec, -1
	v_add_u32_e32 v114, s28, v114
	s_bcnt1_i32_b64 s28, s[24:25]
	v_mbcnt_lo_u32_b32 v111, s24, v114
	v_mbcnt_hi_u32_b32 v111, s25, v111
	v_add_u32_e32 v113, 0xb02, v109
	v_lshl_add_u32 v112, v111, 2, s89
	v_cmp_gt_u32_e64 s[36:37], s29, v111
	s_nop 0
	s_and_b64 s[36:37], s[36:37], s[24:25]
	s_mov_b64 exec, s[36:37]
	ds_write_b32 v112, v113
	s_mov_b64 exec, -1
	v_add_u32_e32 v114, s28, v114
	s_bcnt1_i32_b64 s28, s[26:27]
	v_mbcnt_lo_u32_b32 v111, s26, v114
	v_mbcnt_hi_u32_b32 v111, s27, v111
	v_add_u32_e32 v113, 0xb03, v109
	v_lshl_add_u32 v112, v111, 2, s89
	v_cmp_gt_u32_e64 s[36:37], s29, v111
	s_nop 0
	s_and_b64 s[36:37], s[36:37], s[26:27]
	s_mov_b64 exec, s[36:37]
	ds_write_b32 v112, v113
	s_mov_b64 exec, -1
	v_add_u32_e32 v114, s28, v114
.Ltk_p2_g11:
	s_cmp_lt_u32 s0, 12
	s_cbranch_scc1 .Ltk_p2_done
	v_cmp_eq_u32_e64 s[20:21], v50, v110
	v_cmp_eq_u32_e64 s[22:23], v51, v110
	v_cmp_eq_u32_e64 s[24:25], v52, v110
	v_cmp_eq_u32_e64 s[26:27], v53, v110
	s_or_b64 s[36:37], s[20:21], s[22:23]
	s_or_b64 s[30:31], s[24:25], s[26:27]
	s_or_b64 s[36:37], s[36:37], s[30:31]
	s_cbranch_scc0 .Ltk_p2_g12
	s_bcnt1_i32_b64 s28, s[20:21]
	v_mbcnt_lo_u32_b32 v111, s20, v114
	v_mbcnt_hi_u32_b32 v111, s21, v111
	v_add_u32_e32 v113, 0xc00, v109
	v_lshl_add_u32 v112, v111, 2, s89
	v_cmp_gt_u32_e64 s[36:37], s29, v111
	s_nop 0
	s_and_b64 s[36:37], s[36:37], s[20:21]
	s_mov_b64 exec, s[36:37]
	ds_write_b32 v112, v113
	s_mov_b64 exec, -1
	v_add_u32_e32 v114, s28, v114
	s_bcnt1_i32_b64 s28, s[22:23]
	v_mbcnt_lo_u32_b32 v111, s22, v114
	v_mbcnt_hi_u32_b32 v111, s23, v111
	v_add_u32_e32 v113, 0xc01, v109
	v_lshl_add_u32 v112, v111, 2, s89
	v_cmp_gt_u32_e64 s[36:37], s29, v111
	s_nop 0
	s_and_b64 s[36:37], s[36:37], s[22:23]
	s_mov_b64 exec, s[36:37]
	ds_write_b32 v112, v113
	s_mov_b64 exec, -1
	v_add_u32_e32 v114, s28, v114
	s_bcnt1_i32_b64 s28, s[24:25]
	v_mbcnt_lo_u32_b32 v111, s24, v114
	v_mbcnt_hi_u32_b32 v111, s25, v111
	v_add_u32_e32 v113, 0xc02, v109
	v_lshl_add_u32 v112, v111, 2, s89
	v_cmp_gt_u32_e64 s[36:37], s29, v111
	s_nop 0
	s_and_b64 s[36:37], s[36:37], s[24:25]
	s_mov_b64 exec, s[36:37]
	ds_write_b32 v112, v113
	s_mov_b64 exec, -1
	v_add_u32_e32 v114, s28, v114
	s_bcnt1_i32_b64 s28, s[26:27]
	v_mbcnt_lo_u32_b32 v111, s26, v114
	v_mbcnt_hi_u32_b32 v111, s27, v111
	v_add_u32_e32 v113, 0xc03, v109
	v_lshl_add_u32 v112, v111, 2, s89
	v_cmp_gt_u32_e64 s[36:37], s29, v111
	s_nop 0
	s_and_b64 s[36:37], s[36:37], s[26:27]
	s_mov_b64 exec, s[36:37]
	ds_write_b32 v112, v113
	s_mov_b64 exec, -1
	v_add_u32_e32 v114, s28, v114
.Ltk_p2_g12:
	s_cmp_lt_u32 s0, 13
	s_cbranch_scc1 .Ltk_p2_done
	v_cmp_eq_u32_e64 s[20:21], v54, v110
	v_cmp_eq_u32_e64 s[22:23], v55, v110
	v_cmp_eq_u32_e64 s[24:25], v56, v110
	v_cmp_eq_u32_e64 s[26:27], v57, v110
	s_or_b64 s[36:37], s[20:21], s[22:23]
	s_or_b64 s[30:31], s[24:25], s[26:27]
	s_or_b64 s[36:37], s[36:37], s[30:31]
	s_cbranch_scc0 .Ltk_p2_g13
	s_bcnt1_i32_b64 s28, s[20:21]
	v_mbcnt_lo_u32_b32 v111, s20, v114
	v_mbcnt_hi_u32_b32 v111, s21, v111
	v_add_u32_e32 v113, 0xd00, v109
	v_lshl_add_u32 v112, v111, 2, s89
	v_cmp_gt_u32_e64 s[36:37], s29, v111
	s_nop 0
	s_and_b64 s[36:37], s[36:37], s[20:21]
	s_mov_b64 exec, s[36:37]
	ds_write_b32 v112, v113
	s_mov_b64 exec, -1
	v_add_u32_e32 v114, s28, v114
	s_bcnt1_i32_b64 s28, s[22:23]
	v_mbcnt_lo_u32_b32 v111, s22, v114
	v_mbcnt_hi_u32_b32 v111, s23, v111
	v_add_u32_e32 v113, 0xd01, v109
	v_lshl_add_u32 v112, v111, 2, s89
	v_cmp_gt_u32_e64 s[36:37], s29, v111
	s_nop 0
	s_and_b64 s[36:37], s[36:37], s[22:23]
	s_mov_b64 exec, s[36:37]
	ds_write_b32 v112, v113
	s_mov_b64 exec, -1
	v_add_u32_e32 v114, s28, v114
	s_bcnt1_i32_b64 s28, s[24:25]
	v_mbcnt_lo_u32_b32 v111, s24, v114
	v_mbcnt_hi_u32_b32 v111, s25, v111
	v_add_u32_e32 v113, 0xd02, v109
	v_lshl_add_u32 v112, v111, 2, s89
	v_cmp_gt_u32_e64 s[36:37], s29, v111
	s_nop 0
	s_and_b64 s[36:37], s[36:37], s[24:25]
	s_mov_b64 exec, s[36:37]
	ds_write_b32 v112, v113
	s_mov_b64 exec, -1
	v_add_u32_e32 v114, s28, v114
	s_bcnt1_i32_b64 s28, s[26:27]
	v_mbcnt_lo_u32_b32 v111, s26, v114
	v_mbcnt_hi_u32_b32 v111, s27, v111
	v_add_u32_e32 v113, 0xd03, v109
	v_lshl_add_u32 v112, v111, 2, s89
	v_cmp_gt_u32_e64 s[36:37], s29, v111
	s_nop 0
	s_and_b64 s[36:37], s[36:37], s[26:27]
	s_mov_b64 exec, s[36:37]
	ds_write_b32 v112, v113
	s_mov_b64 exec, -1
	v_add_u32_e32 v114, s28, v114
.Ltk_p2_g13:
	s_cmp_lt_u32 s0, 14
	s_cbranch_scc1 .Ltk_p2_done
	v_cmp_eq_u32_e64 s[20:21], v58, v110
	v_cmp_eq_u32_e64 s[22:23], v59, v110
	v_cmp_eq_u32_e64 s[24:25], v60, v110
	v_cmp_eq_u32_e64 s[26:27], v61, v110
	s_or_b64 s[36:37], s[20:21], s[22:23]
	s_or_b64 s[30:31], s[24:25], s[26:27]
	s_or_b64 s[36:37], s[36:37], s[30:31]
	s_cbranch_scc0 .Ltk_p2_g14
	s_bcnt1_i32_b64 s28, s[20:21]
	v_mbcnt_lo_u32_b32 v111, s20, v114
	v_mbcnt_hi_u32_b32 v111, s21, v111
	v_add_u32_e32 v113, 0xe00, v109
	v_lshl_add_u32 v112, v111, 2, s89
	v_cmp_gt_u32_e64 s[36:37], s29, v111
	s_nop 0
	s_and_b64 s[36:37], s[36:37], s[20:21]
	s_mov_b64 exec, s[36:37]
	ds_write_b32 v112, v113
	s_mov_b64 exec, -1
	v_add_u32_e32 v114, s28, v114
	s_bcnt1_i32_b64 s28, s[22:23]
	v_mbcnt_lo_u32_b32 v111, s22, v114
	v_mbcnt_hi_u32_b32 v111, s23, v111
	v_add_u32_e32 v113, 0xe01, v109
	v_lshl_add_u32 v112, v111, 2, s89
	v_cmp_gt_u32_e64 s[36:37], s29, v111
	s_nop 0
	s_and_b64 s[36:37], s[36:37], s[22:23]
	s_mov_b64 exec, s[36:37]
	ds_write_b32 v112, v113
	s_mov_b64 exec, -1
	v_add_u32_e32 v114, s28, v114
	s_bcnt1_i32_b64 s28, s[24:25]
	v_mbcnt_lo_u32_b32 v111, s24, v114
	v_mbcnt_hi_u32_b32 v111, s25, v111
	v_add_u32_e32 v113, 0xe02, v109
	v_lshl_add_u32 v112, v111, 2, s89
	v_cmp_gt_u32_e64 s[36:37], s29, v111
	s_nop 0
	s_and_b64 s[36:37], s[36:37], s[24:25]
	s_mov_b64 exec, s[36:37]
	ds_write_b32 v112, v113
	s_mov_b64 exec, -1
	v_add_u32_e32 v114, s28, v114
	s_bcnt1_i32_b64 s28, s[26:27]
	v_mbcnt_lo_u32_b32 v111, s26, v114
	v_mbcnt_hi_u32_b32 v111, s27, v111
	v_add_u32_e32 v113, 0xe03, v109
	v_lshl_add_u32 v112, v111, 2, s89
	v_cmp_gt_u32_e64 s[36:37], s29, v111
	s_nop 0
	s_and_b64 s[36:37], s[36:37], s[26:27]
	s_mov_b64 exec, s[36:37]
	ds_write_b32 v112, v113
	s_mov_b64 exec, -1
	v_add_u32_e32 v114, s28, v114
.Ltk_p2_g14:
	s_cmp_lt_u32 s0, 15
	s_cbranch_scc1 .Ltk_p2_done
	v_cmp_eq_u32_e64 s[20:21], v62, v110
	v_cmp_eq_u32_e64 s[22:23], v63, v110
	v_cmp_eq_u32_e64 s[24:25], v64, v110
	v_cmp_eq_u32_e64 s[26:27], v65, v110
	s_or_b64 s[36:37], s[20:21], s[22:23]
	s_or_b64 s[30:31], s[24:25], s[26:27]
	s_or_b64 s[36:37], s[36:37], s[30:31]
	s_cbranch_scc0 .Ltk_p2_g15
	s_bcnt1_i32_b64 s28, s[20:21]
	v_mbcnt_lo_u32_b32 v111, s20, v114
	v_mbcnt_hi_u32_b32 v111, s21, v111
	v_add_u32_e32 v113, 0xf00, v109
	v_lshl_add_u32 v112, v111, 2, s89
	v_cmp_gt_u32_e64 s[36:37], s29, v111
	s_nop 0
	s_and_b64 s[36:37], s[36:37], s[20:21]
	s_mov_b64 exec, s[36:37]
	ds_write_b32 v112, v113
	s_mov_b64 exec, -1
	v_add_u32_e32 v114, s28, v114
	s_bcnt1_i32_b64 s28, s[22:23]
	v_mbcnt_lo_u32_b32 v111, s22, v114
	v_mbcnt_hi_u32_b32 v111, s23, v111
	v_add_u32_e32 v113, 0xf01, v109
	v_lshl_add_u32 v112, v111, 2, s89
	v_cmp_gt_u32_e64 s[36:37], s29, v111
	s_nop 0
	s_and_b64 s[36:37], s[36:37], s[22:23]
	s_mov_b64 exec, s[36:37]
	ds_write_b32 v112, v113
	s_mov_b64 exec, -1
	v_add_u32_e32 v114, s28, v114
	s_bcnt1_i32_b64 s28, s[24:25]
	v_mbcnt_lo_u32_b32 v111, s24, v114
	v_mbcnt_hi_u32_b32 v111, s25, v111
	v_add_u32_e32 v113, 0xf02, v109
	v_lshl_add_u32 v112, v111, 2, s89
	v_cmp_gt_u32_e64 s[36:37], s29, v111
	s_nop 0
	s_and_b64 s[36:37], s[36:37], s[24:25]
	s_mov_b64 exec, s[36:37]
	ds_write_b32 v112, v113
	s_mov_b64 exec, -1
	v_add_u32_e32 v114, s28, v114
	s_bcnt1_i32_b64 s28, s[26:27]
	v_mbcnt_lo_u32_b32 v111, s26, v114
	v_mbcnt_hi_u32_b32 v111, s27, v111
	v_add_u32_e32 v113, 0xf03, v109
	v_lshl_add_u32 v112, v111, 2, s89
	v_cmp_gt_u32_e64 s[36:37], s29, v111
	s_nop 0
	s_and_b64 s[36:37], s[36:37], s[26:27]
	s_mov_b64 exec, s[36:37]
	ds_write_b32 v112, v113
	s_mov_b64 exec, -1
	v_add_u32_e32 v114, s28, v114
.Ltk_p2_g15:
.Ltk_p2_done:
.Ltk_fin:
	v_mov_b32_e32 v172, 0x100
	s_mov_b64 s[2:3], -1
	s_branch .LBB0_1123

.Lcv_a_nop:
	s_waitcnt lgkmcnt(0)
	v_add_u32_e32 v2, 31, v172
	v_and_b32_e32 v173, 15, v151
	v_ashrrev_i32_e32 v174, 4, v151
	v_ashrrev_i32_e32 v176, 5, v2
	v_mov_b32_e32 v29, 0
	v_lshlrev_b32_e32 v148, 7, v173
	v_mov_b32_e32 v149, v147
	v_cmp_lt_i32_e32 vcc, 0, v176
	v_lshlrev_b32_e32 v150, 2, v174
	v_mov_b32_e32 v28, v29
	v_mov_b32_e32 v27, v29
	v_mov_b32_e32 v26, v29
	v_mov_b32_e32 v33, v29
	v_mov_b32_e32 v32, v29
	v_mov_b32_e32 v31, v29
	v_mov_b32_e32 v30, v29
	v_mov_b32_e32 v25, v29
	v_mov_b32_e32 v24, v29
	v_mov_b32_e32 v23, v29
	v_mov_b32_e32 v22, v29
	v_mov_b32_e32 v21, v29
	v_mov_b32_e32 v20, v29
	v_mov_b32_e32 v19, v29
	v_mov_b32_e32 v18, v29
	v_mov_b32_e32 v17, v29
	v_mov_b32_e32 v16, v29
	v_mov_b32_e32 v15, v29
	v_mov_b32_e32 v14, v29
	v_mov_b32_e32 v13, v29
	v_mov_b32_e32 v12, v29
	v_mov_b32_e32 v11, v29
	v_mov_b32_e32 v10, v29
	v_mov_b32_e32 v9, v29
	v_mov_b32_e32 v8, v29
	v_mov_b32_e32 v7, v29
	v_mov_b32_e32 v6, v29
	v_mov_b32_e32 v5, v29
	v_mov_b32_e32 v4, v29
	v_mov_b32_e32 v3, v29
	v_mov_b32_e32 v2, v29
	v_mov_b32_e32 v179, v29
	s_and_saveexec_b64 s[0:1], vcc
	s_cbranch_execz .LBB0_1127
	v_readfirstlane_b32 s10, v176
	v_readfirstlane_b32 s36, v172
	v_readlane_b32 s37, v242, 49
	s_mul_i32 s5, s78, 0x3400000
	s_mul_hi_i32 s4, s78, 0x3400000
	s_add_u32 s2, s82, s5
	s_addc_u32 s3, s83, s4
	s_add_u32 s4, s2, 0x2800
	s_addc_u32 s5, s3, 0
	s_add_u32 s6, s2, 0x2900
	s_addc_u32 s7, s3, 0
	s_mul_i32 s20, s97, 0x3400
	s_mul_hi_u32 s21, s96, 0x3400
	s_add_i32 s21, s21, s20
	s_mul_i32 s20, s96, 0x3400
	s_add_u32 s20, s82, s20
	s_addc_u32 s21, s83, s21
	s_add_u32 s20, s20, 0x1800
	s_addc_u32 s21, s21, 0
	s_add_u32 s26, s89, 0x400
	s_lshl_b32 s27, s37, 13
	s_add_u32 s27, s27, 0x14000
	v_lshlrev_b32_e32 v96, 2, v150
	v_lshl_add_u32 v153, v148, 1, v96
	global_load_dwordx4 v[42:45], v153, s[20:21]
	global_load_dwordx4 v[34:37], v153, s[20:21] offset:64
	global_load_dwordx4 v[38:41], v153, s[20:21] offset:128
	global_load_dwordx4 v[46:49], v153, s[20:21] offset:192
	v_add_u32_e32 v239, s89, v150
	ds_read2_b32 v[98:99], v239 offset0:0 offset1:4
	ds_read2_b32 v[100:101], v239 offset0:8 offset1:12
	ds_read2_b32 v[102:103], v239 offset0:16 offset1:20
	ds_read2_b32 v[104:105], v239 offset0:24 offset1:28
	ds_read2_b32 v[106:107], v239 offset0:32 offset1:36
	ds_read2_b32 v[108:109], v239 offset0:40 offset1:44
	ds_read2_b32 v[110:111], v239 offset0:48 offset1:52
	ds_read2_b32 v[112:113], v239 offset0:56 offset1:60
	v_mov_b32_e32 v96, v174
	v_xor_b32_e32 v96, v96, v173
	v_lshlrev_b32_e32 v220, 4, v96
	v_add_u32_e32 v96, 4, v174
	v_xor_b32_e32 v96, v96, v173
	v_lshlrev_b32_e32 v221, 4, v96
	v_add_u32_e32 v96, 8, v174
	v_xor_b32_e32 v96, v96, v173
	v_lshlrev_b32_e32 v222, 4, v96
	v_add_u32_e32 v96, 12, v174
	v_xor_b32_e32 v96, v96, v173
	v_lshlrev_b32_e32 v223, 4, v96
	v_lshlrev_b32_e32 v224, 4, v173
	v_lshlrev_b32_e32 v96, 1, v174
	v_xor_b32_e32 v96, v96, v173
	v_lshlrev_b32_e32 v96, 4, v96
	v_lshl_add_u32 v97, v174, 8, s27
	v_add_u32_e32 v225, v97, v96
	v_xor_b32_e32 v96, 0x80, v96
	v_add_u32_e32 v226, v97, v96
	v_lshl_add_u32 v97, v173, 8, s26
	v_mov_b32_e32 v96, v174
	v_xor_b32_e32 v96, v96, v173
	v_lshl_add_u32 v227, v96, 4, v97
	v_add_u32_e32 v96, 4, v174
	v_xor_b32_e32 v96, v96, v173
	v_lshl_add_u32 v228, v96, 4, v97
	v_add_u32_e32 v96, 8, v174
	v_xor_b32_e32 v96, v96, v173
	v_lshl_add_u32 v229, v96, 4, v97
	v_add_u32_e32 v96, 12, v174
	v_xor_b32_e32 v96, v96, v173
	v_lshl_add_u32 v230, v96, 4, v97
	v_lshrrev_b32_e32 v241, 2, v173
	v_add_u32_e32 v241, v241, v150
	v_and_b32_e32 v177, 7, v241
	v_and_b32_e32 v96, 3, v173
	v_lshlrev_b32_e32 v96, 3, v96
	v_lshl_add_u32 v241, v241, 8, v96
	v_add_u32_e32 v241, s27, v241
	v_xor_b32_e32 v96, 0, v177
	v_lshl_add_u32 v231, v96, 5, v241
	v_xor_b32_e32 v96, 1, v177
	v_lshl_add_u32 v232, v96, 5, v241
	v_xor_b32_e32 v96, 2, v177
	v_lshl_add_u32 v233, v96, 5, v241
	v_xor_b32_e32 v96, 3, v177
	v_lshl_add_u32 v234, v96, 5, v241
	v_xor_b32_e32 v96, 4, v177
	v_lshl_add_u32 v235, v96, 5, v241
	v_xor_b32_e32 v96, 5, v177
	v_lshl_add_u32 v236, v96, 5, v241
	v_xor_b32_e32 v96, 6, v177
	v_lshl_add_u32 v237, v96, 5, v241
	v_xor_b32_e32 v96, 7, v177
	v_lshl_add_u32 v238, v96, 5, v241
	v_mov_b32_e32 v2, 0
	v_mov_b32_e32 v3, 0
	v_mov_b32_e32 v4, 0
	v_mov_b32_e32 v5, 0
	v_mov_b32_e32 v6, 0
	v_mov_b32_e32 v7, 0
	v_mov_b32_e32 v8, 0
	v_mov_b32_e32 v9, 0
	v_mov_b32_e32 v10, 0
	v_mov_b32_e32 v11, 0
	v_mov_b32_e32 v12, 0
	v_mov_b32_e32 v13, 0
	v_mov_b32_e32 v14, 0
	v_mov_b32_e32 v15, 0
	v_mov_b32_e32 v16, 0
	v_mov_b32_e32 v17, 0
	v_mov_b32_e32 v18, 0
	v_mov_b32_e32 v19, 0
	v_mov_b32_e32 v20, 0
	v_mov_b32_e32 v21, 0
	v_mov_b32_e32 v22, 0
	v_mov_b32_e32 v23, 0
	v_mov_b32_e32 v24, 0
	v_mov_b32_e32 v25, 0
	v_mov_b32_e32 v26, 0
	v_mov_b32_e32 v27, 0
	v_mov_b32_e32 v28, 0
	v_mov_b32_e32 v29, 0
	v_mov_b32_e32 v30, 0
	v_mov_b32_e32 v31, 0
	v_mov_b32_e32 v32, 0
	v_mov_b32_e32 v33, 0
	v_mov_b32_e32 v179, 0
	v_mov_b32_e32 v181, 0xf149f2ca
	v_mov_b32_e32 v95, 0
	s_mov_b32 s11, 0
	s_mov_b32 s22, 0
	s_waitcnt lgkmcnt(0)
	s_mov_b32 m0, s26
	v_mad_u32_u24 v240, v98, s35, v220
	global_load_lds_dwordx4 v240, s[4:5]
	s_add_u32 m0, s26, 1024
	v_mad_u32_u24 v240, v99, s35, v221
	global_load_lds_dwordx4 v240, s[4:5]
	s_add_u32 m0, s26, 2048
	v_mad_u32_u24 v240, v100, s35, v222
	global_load_lds_dwordx4 v240, s[4:5]
	s_add_u32 m0, s26, 3072
	v_mad_u32_u24 v240, v101, s35, v223
	global_load_lds_dwordx4 v240, s[4:5]
	s_add_u32 m0, s26, 4096
	v_mad_u32_u24 v240, v102, s35, v220
	global_load_lds_dwordx4 v240, s[4:5]
	s_add_u32 m0, s26, 5120
	v_mad_u32_u24 v240, v103, s35, v221
	global_load_lds_dwordx4 v240, s[4:5]
	s_add_u32 m0, s26, 6144
	v_mad_u32_u24 v240, v104, s35, v222
	global_load_lds_dwordx4 v240, s[4:5]
	s_add_u32 m0, s26, 7168
	v_mad_u32_u24 v240, v105, s35, v223
	global_load_lds_dwordx4 v240, s[4:5]
	v_mad_u32_u24 v240, v98, s35, v224
	global_load_dwordx4 v[114:117], v240, s[6:7]
	v_mad_u32_u24 v240, v99, s35, v224
	global_load_dwordx4 v[118:121], v240, s[6:7]
	v_mad_u32_u24 v240, v100, s35, v224
	global_load_dwordx4 v[122:125], v240, s[6:7]
	v_mad_u32_u24 v240, v101, s35, v224
	global_load_dwordx4 v[126:129], v240, s[6:7]
	v_mad_u32_u24 v240, v102, s35, v224
	global_load_dwordx4 v[130:133], v240, s[6:7]
	v_mad_u32_u24 v240, v103, s35, v224
	global_load_dwordx4 v[134:137], v240, s[6:7]
	v_mad_u32_u24 v240, v104, s35, v224
	global_load_dwordx4 v[138:141], v240, s[6:7]
	v_mad_u32_u24 v240, v105, s35, v224
	global_load_dwordx4 v[142:145], v240, s[6:7]
	s_cmp_ge_u32 s10, 2
	s_cbranch_scc0 .Lat_A
	v_mad_u32_u24 v240, v106, s35, v224
	global_load_dwordx4 v[188:191], v240, s[6:7]
	v_mad_u32_u24 v240, v107, s35, v224
	global_load_dwordx4 v[192:195], v240, s[6:7]
	v_mad_u32_u24 v240, v108, s35, v224
	global_load_dwordx4 v[196:199], v240, s[6:7]
	v_mad_u32_u24 v240, v109, s35, v224
	global_load_dwordx4 v[200:203], v240, s[6:7]
	v_mad_u32_u24 v240, v110, s35, v224
	global_load_dwordx4 v[204:207], v240, s[6:7]
	v_mad_u32_u24 v240, v111, s35, v224
	global_load_dwordx4 v[208:211], v240, s[6:7]
	v_mad_u32_u24 v240, v112, s35, v224
	global_load_dwordx4 v[212:215], v240, s[6:7]
	v_mad_u32_u24 v240, v113, s35, v224
	global_load_dwordx4 v[216:219], v240, s[6:7]
.Lat_A:
	s_sub_u32 s23, s10, s11
	s_cmp_ge_u32 s23, 2
	s_cbranch_scc1 .Lat_A_w8
	s_waitcnt vmcnt(0)
	s_branch .Lat_A_go
.Lat_A_w8:
	s_waitcnt vmcnt(8)
.Lat_A_go:
	ds_read_b128 v[50:53], v227
	ds_read_b128 v[66:69], v227 offset:4096
	ds_read_b128 v[54:57], v228
	ds_read_b128 v[70:73], v228 offset:4096
	ds_read_b128 v[58:61], v229
	ds_read_b128 v[74:77], v229 offset:4096
	ds_read_b128 v[62:65], v230
	ds_read_b128 v[78:81], v230 offset:4096
	ds_write_b128 v225, v[114:117]
	ds_write_b128 v226, v[118:121] offset:1024
	ds_write_b128 v225, v[122:125] offset:2048
	ds_write_b128 v226, v[126:129] offset:3072
	ds_write_b128 v225, v[130:133] offset:4096
	ds_write_b128 v226, v[134:137] offset:5120
	ds_write_b128 v225, v[138:141] offset:6144
	ds_write_b128 v226, v[142:145] offset:7168
	s_cmp_ge_u32 s23, 3
	s_cbranch_scc0 .Lat_A_nosel
	ds_read2_b32 v[98:99], v239 offset0:64 offset1:68
	ds_read2_b32 v[100:101], v239 offset0:72 offset1:76
	ds_read2_b32 v[102:103], v239 offset0:80 offset1:84
	ds_read2_b32 v[104:105], v239 offset0:88 offset1:92
.Lat_A_nosel:
	s_waitcnt lgkmcnt(0)
	s_cmp_ge_u32 s23, 2
	s_cbranch_scc0 .Lat_A_nok
	s_mov_b32 m0, s26
	v_mad_u32_u24 v240, v106, s35, v220
	global_load_lds_dwordx4 v240, s[4:5]
	s_add_u32 m0, s26, 1024
	v_mad_u32_u24 v240, v107, s35, v221
	global_load_lds_dwordx4 v240, s[4:5]
	s_add_u32 m0, s26, 2048
	v_mad_u32_u24 v240, v108, s35, v222
	global_load_lds_dwordx4 v240, s[4:5]
	s_add_u32 m0, s26, 3072
	v_mad_u32_u24 v240, v109, s35, v223
	global_load_lds_dwordx4 v240, s[4:5]
	s_add_u32 m0, s26, 4096
	v_mad_u32_u24 v240, v110, s35, v220
	global_load_lds_dwordx4 v240, s[4:5]
	s_add_u32 m0, s26, 5120
	v_mad_u32_u24 v240, v111, s35, v221
	global_load_lds_dwordx4 v240, s[4:5]
	s_add_u32 m0, s26, 6144
	v_mad_u32_u24 v240, v112, s35, v222
	global_load_lds_dwordx4 v240, s[4:5]
	s_add_u32 m0, s26, 7168
	v_mad_u32_u24 v240, v113, s35, v223
	global_load_lds_dwordx4 v240, s[4:5]
	s_cmp_ge_u32 s23, 3
	s_cbranch_scc0 .Lat_A_nok
	v_mad_u32_u24 v240, v98, s35, v224
	global_load_dwordx4 v[114:117], v240, s[6:7]
	v_mad_u32_u24 v240, v99, s35, v224
	global_load_dwordx4 v[118:121], v240, s[6:7]
	v_mad_u32_u24 v240, v100, s35, v224
	global_load_dwordx4 v[122:125], v240, s[6:7]
	v_mad_u32_u24 v240, v101, s35, v224
	global_load_dwordx4 v[126:129], v240, s[6:7]
	v_mad_u32_u24 v240, v102, s35, v224
	global_load_dwordx4 v[130:133], v240, s[6:7]
	v_mad_u32_u24 v240, v103, s35, v224
	global_load_dwordx4 v[134:137], v240, s[6:7]
	v_mad_u32_u24 v240, v104, s35, v224
	global_load_dwordx4 v[138:141], v240, s[6:7]
	v_mad_u32_u24 v240, v105, s35, v224
	global_load_dwordx4 v[142:145], v240, s[6:7]
.Lat_A_nok:
	v_mfma_f32_16x16x32_bf16 v[82:85], v[50:53], v[42:45], 0
	v_mfma_f32_16x16x32_bf16 v[86:89], v[66:69], v[42:45], 0
	v_mfma_f32_16x16x32_bf16 v[82:85], v[54:57], v[34:37], v[82:85]
	v_mfma_f32_16x16x32_bf16 v[86:89], v[70:73], v[34:37], v[86:89]
	v_mfma_f32_16x16x32_bf16 v[82:85], v[58:61], v[38:41], v[82:85]
	v_mfma_f32_16x16x32_bf16 v[86:89], v[74:77], v[38:41], v[86:89]
	v_mfma_f32_16x16x32_bf16 v[82:85], v[62:65], v[46:49], v[82:85]
	v_mfma_f32_16x16x32_bf16 v[86:89], v[78:81], v[46:49], v[86:89]
	v_add_u32_e32 v90, s22, v150
	v_add_u32_e32 v91, 16, v90
	s_add_u32 s24, s22, 32
	s_nop 6
	v_mul_f32_e32 v82, 0x3e0293ee, v82
	v_mul_f32_e32 v83, 0x3e0293ee, v83
	v_mul_f32_e32 v84, 0x3e0293ee, v84
	v_mul_f32_e32 v85, 0x3e0293ee, v85
	v_mul_f32_e32 v86, 0x3e0293ee, v86
	v_mul_f32_e32 v87, 0x3e0293ee, v87
	v_mul_f32_e32 v88, 0x3e0293ee, v88
	v_mul_f32_e32 v89, 0x3e0293ee, v89
	s_cmp_le_u32 s24, s36
	s_cbranch_scc1 .Lat_A_full
	v_add_u32_e32 v92, 0, v90
	v_cmp_lt_i32_e32 vcc, v92, v172
	v_add_u32_e32 v93, 0, v91
	s_nop 1
	v_cndmask_b32_e32 v82, v170, v82, vcc
	v_cmp_lt_i32_e32 vcc, v93, v172
	s_nop 1
	s_nop 0
	v_cndmask_b32_e32 v86, v170, v86, vcc
	v_add_u32_e32 v92, 1, v90
	v_cmp_lt_i32_e32 vcc, v92, v172
	v_add_u32_e32 v93, 1, v91
	s_nop 1
	v_cndmask_b32_e32 v83, v170, v83, vcc
	v_cmp_lt_i32_e32 vcc, v93, v172
	s_nop 1
	s_nop 0
	v_cndmask_b32_e32 v87, v170, v87, vcc
	v_add_u32_e32 v92, 2, v90
	v_cmp_lt_i32_e32 vcc, v92, v172
	v_add_u32_e32 v93, 2, v91
	s_nop 1
	v_cndmask_b32_e32 v84, v170, v84, vcc
	v_cmp_lt_i32_e32 vcc, v93, v172
	s_nop 1
	s_nop 0
	v_cndmask_b32_e32 v88, v170, v88, vcc
	v_add_u32_e32 v92, 3, v90
	v_cmp_lt_i32_e32 vcc, v92, v172
	v_add_u32_e32 v93, 3, v91
	s_nop 1
	v_cndmask_b32_e32 v85, v170, v85, vcc
	v_cmp_lt_i32_e32 vcc, v93, v172
	s_nop 1
	s_nop 0
	v_cndmask_b32_e32 v89, v170, v89, vcc
.Lat_A_full:
	v_max3_f32 v92, v82, v83, v84
	v_max3_f32 v93, v85, v86, v87
	v_max3_f32 v92, v92, v88, v89
	v_max_f32_e32 v92, v92, v93
	ds_bpermute_b32 v93, v161, v92
	s_waitcnt lgkmcnt(0)
	v_max_f32_e32 v92, v92, v93
	ds_bpermute_b32 v93, v162, v92
	s_waitcnt lgkmcnt(0)
	v_max3_f32 v180, v181, v92, v93
	v_sub_f32_e32 v94, v181, v180
	v_sub_f32_e32 v82, v82, v180
	v_sub_f32_e32 v83, v83, v180
	v_sub_f32_e32 v84, v84, v180
	v_sub_f32_e32 v85, v85, v180
	v_sub_f32_e32 v86, v86, v180
	v_sub_f32_e32 v87, v87, v180
	v_sub_f32_e32 v88, v88, v180
	v_sub_f32_e32 v89, v89, v180
	v_exp_f32_e32 v94, v94
	v_exp_f32_e32 v82, v82
	v_exp_f32_e32 v83, v83
	v_exp_f32_e32 v84, v84
	v_exp_f32_e32 v85, v85
	v_exp_f32_e32 v86, v86
	v_exp_f32_e32 v87, v87
	v_exp_f32_e32 v88, v88
	v_exp_f32_e32 v89, v89
	v_add_f32_e32 v92, v82, v83
	v_add_f32_e32 v93, v84, v85
	v_add_f32_e32 v97, v86, v87
	v_add_f32_e32 v92, v92, v93
	v_add_f32_e32 v96, v88, v89
	v_add_f32_e32 v97, v97, v96
	v_add_f32_e32 v92, v92, v97
	v_mov_b32_e32 v181, v180
	ds_bpermute_b32 v93, v161, v92
	v_cvt_pk_bf16_f32 v82, v82, v83
	v_cvt_pk_bf16_f32 v83, v84, v85
	v_cvt_pk_bf16_f32 v84, v86, v87
	v_cvt_pk_bf16_f32 v85, v88, v89
	v_pk_mul_f32 v[2:3], v[2:3], v[94:95] op_sel_hi:[1,0]
	v_pk_mul_f32 v[4:5], v[4:5], v[94:95] op_sel_hi:[1,0]
	v_pk_mul_f32 v[6:7], v[6:7], v[94:95] op_sel_hi:[1,0]
	v_pk_mul_f32 v[8:9], v[8:9], v[94:95] op_sel_hi:[1,0]
	v_pk_mul_f32 v[10:11], v[10:11], v[94:95] op_sel_hi:[1,0]
	v_pk_mul_f32 v[12:13], v[12:13], v[94:95] op_sel_hi:[1,0]
	v_pk_mul_f32 v[14:15], v[14:15], v[94:95] op_sel_hi:[1,0]
	v_pk_mul_f32 v[16:17], v[16:17], v[94:95] op_sel_hi:[1,0]
	s_waitcnt lgkmcnt(0)
	v_add_f32_e32 v92, v92, v93
	ds_bpermute_b32 v93, v162, v92
	v_pk_mul_f32 v[18:19], v[18:19], v[94:95] op_sel_hi:[1,0]
	v_pk_mul_f32 v[20:21], v[20:21], v[94:95] op_sel_hi:[1,0]
	v_pk_mul_f32 v[22:23], v[22:23], v[94:95] op_sel_hi:[1,0]
	v_pk_mul_f32 v[24:25], v[24:25], v[94:95] op_sel_hi:[1,0]
	v_pk_mul_f32 v[26:27], v[26:27], v[94:95] op_sel_hi:[1,0]
	v_pk_mul_f32 v[28:29], v[28:29], v[94:95] op_sel_hi:[1,0]
	v_pk_mul_f32 v[30:31], v[30:31], v[94:95] op_sel_hi:[1,0]
	v_pk_mul_f32 v[32:33], v[32:33], v[94:95] op_sel_hi:[1,0]
	s_waitcnt lgkmcnt(0)
	v_add_f32_e32 v92, v92, v93
	v_fma_f32 v179, v179, v94, v92
	ds_read_b64_tr_b16 v[86:87], v231
	ds_read_b64_tr_b16 v[88:89], v231 offset:4096
	ds_read_b64_tr_b16 v[244:245], v232
	ds_read_b64_tr_b16 v[246:247], v232 offset:4096
	s_waitcnt lgkmcnt(2)
	v_mfma_f32_16x16x32_bf16 v[2:5], v[86:89], v[82:85], v[2:5]
	ds_read_b64_tr_b16 v[86:87], v233
	ds_read_b64_tr_b16 v[88:89], v233 offset:4096
	s_waitcnt lgkmcnt(2)
	v_mfma_f32_16x16x32_bf16 v[6:9], v[244:247], v[82:85], v[6:9]
	ds_read_b64_tr_b16 v[244:245], v234
	ds_read_b64_tr_b16 v[246:247], v234 offset:4096
	s_waitcnt lgkmcnt(2)
	v_mfma_f32_16x16x32_bf16 v[10:13], v[86:89], v[82:85], v[10:13]
	ds_read_b64_tr_b16 v[86:87], v235
	ds_read_b64_tr_b16 v[88:89], v235 offset:4096
	s_waitcnt lgkmcnt(2)
	v_mfma_f32_16x16x32_bf16 v[14:17], v[244:247], v[82:85], v[14:17]
	ds_read_b64_tr_b16 v[244:245], v236
	ds_read_b64_tr_b16 v[246:247], v236 offset:4096
	s_waitcnt lgkmcnt(2)
	v_mfma_f32_16x16x32_bf16 v[18:21], v[86:89], v[82:85], v[18:21]
	ds_read_b64_tr_b16 v[86:87], v237
	ds_read_b64_tr_b16 v[88:89], v237 offset:4096
	s_waitcnt lgkmcnt(2)
	v_mfma_f32_16x16x32_bf16 v[22:25], v[244:247], v[82:85], v[22:25]
	ds_read_b64_tr_b16 v[244:245], v238
	ds_read_b64_tr_b16 v[246:247], v238 offset:4096
	s_waitcnt lgkmcnt(2)
	v_mfma_f32_16x16x32_bf16 v[30:33], v[86:89], v[82:85], v[30:33]
	s_waitcnt lgkmcnt(0)
	v_mfma_f32_16x16x32_bf16 v[26:29], v[244:247], v[82:85], v[26:29]
	s_add_u32 s11, s11, 1
	s_add_u32 s22, s22, 32
	v_add_u32_e32 v239, 0x80, v239
	s_cmp_lt_u32 s11, s10
	s_cbranch_scc0 .Lat_done

.Lat_B_go:
	ds_read_b128 v[50:53], v227
	ds_read_b128 v[66:69], v227 offset:4096
	ds_read_b128 v[54:57], v228
	ds_read_b128 v[70:73], v228 offset:4096
	ds_read_b128 v[58:61], v229
	ds_read_b128 v[74:77], v229 offset:4096
	ds_read_b128 v[62:65], v230
	ds_read_b128 v[78:81], v230 offset:4096
	ds_write_b128 v225, v[188:191]
	ds_write_b128 v226, v[192:195] offset:1024
	ds_write_b128 v225, v[196:199] offset:2048
	ds_write_b128 v226, v[200:203] offset:3072
	ds_write_b128 v225, v[204:207] offset:4096
	ds_write_b128 v226, v[208:211] offset:5120
	ds_write_b128 v225, v[212:215] offset:6144
	ds_write_b128 v226, v[216:219] offset:7168
	s_cmp_ge_u32 s23, 3
	s_cbranch_scc0 .Lat_B_nosel
	ds_read2_b32 v[106:107], v239 offset0:64 offset1:68
	ds_read2_b32 v[108:109], v239 offset0:72 offset1:76
	ds_read2_b32 v[110:111], v239 offset0:80 offset1:84
	ds_read2_b32 v[112:113], v239 offset0:88 offset1:92
.Lat_B_nosel:
	s_waitcnt lgkmcnt(0)
	s_cmp_ge_u32 s23, 2
	s_cbranch_scc0 .Lat_B_nok
	s_mov_b32 m0, s26
	v_mad_u32_u24 v240, v98, s35, v220
	global_load_lds_dwordx4 v240, s[4:5]
	s_add_u32 m0, s26, 1024
	v_mad_u32_u24 v240, v99, s35, v221
	global_load_lds_dwordx4 v240, s[4:5]
	s_add_u32 m0, s26, 2048
	v_mad_u32_u24 v240, v100, s35, v222
	global_load_lds_dwordx4 v240, s[4:5]
	s_add_u32 m0, s26, 3072
	v_mad_u32_u24 v240, v101, s35, v223
	global_load_lds_dwordx4 v240, s[4:5]
	s_add_u32 m0, s26, 4096
	v_mad_u32_u24 v240, v102, s35, v220
	global_load_lds_dwordx4 v240, s[4:5]
	s_add_u32 m0, s26, 5120
	v_mad_u32_u24 v240, v103, s35, v221
	global_load_lds_dwordx4 v240, s[4:5]
	s_add_u32 m0, s26, 6144
	v_mad_u32_u24 v240, v104, s35, v222
	global_load_lds_dwordx4 v240, s[4:5]
	s_add_u32 m0, s26, 7168
	v_mad_u32_u24 v240, v105, s35, v223
	global_load_lds_dwordx4 v240, s[4:5]
	s_cmp_ge_u32 s23, 3
	s_cbranch_scc0 .Lat_B_nok
	v_mad_u32_u24 v240, v106, s35, v224
	global_load_dwordx4 v[188:191], v240, s[6:7]
	v_mad_u32_u24 v240, v107, s35, v224
	global_load_dwordx4 v[192:195], v240, s[6:7]
	v_mad_u32_u24 v240, v108, s35, v224
	global_load_dwordx4 v[196:199], v240, s[6:7]
	v_mad_u32_u24 v240, v109, s35, v224
	global_load_dwordx4 v[200:203], v240, s[6:7]
	v_mad_u32_u24 v240, v110, s35, v224
	global_load_dwordx4 v[204:207], v240, s[6:7]
	v_mad_u32_u24 v240, v111, s35, v224
	global_load_dwordx4 v[208:211], v240, s[6:7]
	v_mad_u32_u24 v240, v112, s35, v224
	global_load_dwordx4 v[212:215], v240, s[6:7]
	v_mad_u32_u24 v240, v113, s35, v224
	global_load_dwordx4 v[216:219], v240, s[6:7]

.Lat_B_full:
	v_max3_f32 v92, v82, v83, v84
	v_max3_f32 v93, v85, v86, v87
	v_max3_f32 v92, v92, v88, v89
	v_max_f32_e32 v92, v92, v93
	ds_bpermute_b32 v93, v161, v92
	s_waitcnt lgkmcnt(0)
	v_max_f32_e32 v92, v92, v93
	ds_bpermute_b32 v93, v162, v92
	s_waitcnt lgkmcnt(0)
	v_max3_f32 v180, v181, v92, v93
	v_sub_f32_e32 v94, v181, v180
	v_sub_f32_e32 v82, v82, v180
	v_sub_f32_e32 v83, v83, v180
	v_sub_f32_e32 v84, v84, v180
	v_sub_f32_e32 v85, v85, v180
	v_sub_f32_e32 v86, v86, v180
	v_sub_f32_e32 v87, v87, v180
	v_sub_f32_e32 v88, v88, v180
	v_sub_f32_e32 v89, v89, v180
	v_exp_f32_e32 v94, v94
	v_exp_f32_e32 v82, v82
	v_exp_f32_e32 v83, v83
	v_exp_f32_e32 v84, v84
	v_exp_f32_e32 v85, v85
	v_exp_f32_e32 v86, v86
	v_exp_f32_e32 v87, v87
	v_exp_f32_e32 v88, v88
	v_exp_f32_e32 v89, v89
	v_add_f32_e32 v92, v82, v83
	v_add_f32_e32 v93, v84, v85
	v_add_f32_e32 v97, v86, v87
	v_add_f32_e32 v92, v92, v93
	v_add_f32_e32 v96, v88, v89
	v_add_f32_e32 v97, v97, v96
	v_add_f32_e32 v92, v92, v97
	v_mov_b32_e32 v181, v180
	ds_bpermute_b32 v93, v161, v92
	v_cvt_pk_bf16_f32 v82, v82, v83
	v_cvt_pk_bf16_f32 v83, v84, v85
	v_cvt_pk_bf16_f32 v84, v86, v87
	v_cvt_pk_bf16_f32 v85, v88, v89
	v_pk_mul_f32 v[2:3], v[2:3], v[94:95] op_sel_hi:[1,0]
	v_pk_mul_f32 v[4:5], v[4:5], v[94:95] op_sel_hi:[1,0]
	v_pk_mul_f32 v[6:7], v[6:7], v[94:95] op_sel_hi:[1,0]
	v_pk_mul_f32 v[8:9], v[8:9], v[94:95] op_sel_hi:[1,0]
	v_pk_mul_f32 v[10:11], v[10:11], v[94:95] op_sel_hi:[1,0]
	v_pk_mul_f32 v[12:13], v[12:13], v[94:95] op_sel_hi:[1,0]
	v_pk_mul_f32 v[14:15], v[14:15], v[94:95] op_sel_hi:[1,0]
	v_pk_mul_f32 v[16:17], v[16:17], v[94:95] op_sel_hi:[1,0]
	s_waitcnt lgkmcnt(0)
	v_add_f32_e32 v92, v92, v93
	ds_bpermute_b32 v93, v162, v92
	v_pk_mul_f32 v[18:19], v[18:19], v[94:95] op_sel_hi:[1,0]
	v_pk_mul_f32 v[20:21], v[20:21], v[94:95] op_sel_hi:[1,0]
	v_pk_mul_f32 v[22:23], v[22:23], v[94:95] op_sel_hi:[1,0]
	v_pk_mul_f32 v[24:25], v[24:25], v[94:95] op_sel_hi:[1,0]
	v_pk_mul_f32 v[26:27], v[26:27], v[94:95] op_sel_hi:[1,0]
	v_pk_mul_f32 v[28:29], v[28:29], v[94:95] op_sel_hi:[1,0]
	v_pk_mul_f32 v[30:31], v[30:31], v[94:95] op_sel_hi:[1,0]
	v_pk_mul_f32 v[32:33], v[32:33], v[94:95] op_sel_hi:[1,0]
	s_waitcnt lgkmcnt(0)
	v_add_f32_e32 v92, v92, v93
	v_fma_f32 v179, v179, v94, v92
	ds_read_b64_tr_b16 v[86:87], v231
	ds_read_b64_tr_b16 v[88:89], v231 offset:4096
	ds_read_b64_tr_b16 v[244:245], v232
	ds_read_b64_tr_b16 v[246:247], v232 offset:4096
	s_waitcnt lgkmcnt(2)
	v_mfma_f32_16x16x32_bf16 v[2:5], v[86:89], v[82:85], v[2:5]
	ds_read_b64_tr_b16 v[86:87], v233
	ds_read_b64_tr_b16 v[88:89], v233 offset:4096
	s_waitcnt lgkmcnt(2)
	v_mfma_f32_16x16x32_bf16 v[6:9], v[244:247], v[82:85], v[6:9]
	ds_read_b64_tr_b16 v[244:245], v234
	ds_read_b64_tr_b16 v[246:247], v234 offset:4096
	s_waitcnt lgkmcnt(2)
	v_mfma_f32_16x16x32_bf16 v[10:13], v[86:89], v[82:85], v[10:13]
	ds_read_b64_tr_b16 v[86:87], v235
	ds_read_b64_tr_b16 v[88:89], v235 offset:4096
	s_waitcnt lgkmcnt(2)
	v_mfma_f32_16x16x32_bf16 v[14:17], v[244:247], v[82:85], v[14:17]
	ds_read_b64_tr_b16 v[244:245], v236
	ds_read_b64_tr_b16 v[246:247], v236 offset:4096
	s_waitcnt lgkmcnt(2)
	v_mfma_f32_16x16x32_bf16 v[18:21], v[86:89], v[82:85], v[18:21]
	ds_read_b64_tr_b16 v[86:87], v237
	ds_read_b64_tr_b16 v[88:89], v237 offset:4096
	s_waitcnt lgkmcnt(2)
	v_mfma_f32_16x16x32_bf16 v[22:25], v[244:247], v[82:85], v[22:25]
	ds_read_b64_tr_b16 v[244:245], v238
	ds_read_b64_tr_b16 v[246:247], v238 offset:4096
	s_waitcnt lgkmcnt(2)
	v_mfma_f32_16x16x32_bf16 v[30:33], v[86:89], v[82:85], v[30:33]
	s_waitcnt lgkmcnt(0)
	v_mfma_f32_16x16x32_bf16 v[26:29], v[244:247], v[82:85], v[26:29]
	s_add_u32 s11, s11, 1
	s_add_u32 s22, s22, 32
	v_add_u32_e32 v239, 0x80, v239
	s_cmp_lt_u32 s11, s10
	s_cbranch_scc1 .Lat_A
